# add streaming (nt) policy to routed-down y stores and to the phase-1a x/ctx loads
# speedup vs baseline: 1.0237x; 1.0153x over previous
; __device__ void phase1a(const Params& p) {
;     ...
;     for (int g = blockIdx.x * NWV + wid; g * 3 < MR; g += nw) {
;         const int R0 = g * 3;
;         float4 v[3][4]; float ss[3]; const float* md[3];
; #pragma unroll
;         for (int j = 0; j < 3; ++j) {
;             const int R = R0 + j; const int Rc = R < MR ? R : R0;
;             const int b = Rc / TT, t = Rc - b * TT;
;             const float* src = t < SEQ ? p.x + (size_t)(b * SEQ + t) * D : p.ctx + (size_t)(b * CTXL + t - SEQ) * D;
;             md[j] = p.mod + (t < SEQ ? b : 4) * 6144;
; #pragma unroll
;             for (int i = 0; i < 4; ++i) v[j][i] = *(const float4*)(src + i * 256 + lane * 4);
;         }
;         float4 mf[4], ma[4]; const float* mcur = md[0];
; #pragma unroll
;         for (int i = 0; i < 4; ++i) {
;             const int k = i * 256 + lane * 4;
;             const float4 n1 = *(const float4*)(p.norm1 + k), sh = *(const float4*)(mcur + k), sc = *(const float4*)(mcur + 1024 + k);
;             mf[i] = make_float4(n1.x * (1.f + sc.x), n1.y * (1.f + sc.y), n1.z * (1.f + sc.z), n1.w * (1.f + sc.w)); ma[i] = sh;
;         }
; #pragma unroll
;         for (int j = 0; j < 3; ++j) {
;             float s_ = 0.f;
; #pragma unroll
;             for (int i = 0; i < 4; ++i) s_ += v[j][i].x * v[j][i].x + v[j][i].y * v[j][i].y + v[j][i].z * v[j][i].z + v[j][i].w * v[j][i].w;
;             ss[j] = s_;
;         }
; #pragma unroll
;         for (int o = 32; o >= 1; o >>= 1) { ss[0] += __shfl_xor(ss[0], o); ss[1] += __shfl_xor(ss[1], o); ss[2] += __shfl_xor(ss[2], o); }
.LBB0_128:
	v_mul_hi_i32 v2, v1, s3
	v_lshrrev_b32_e32 v3, 31, v2
	v_ashrrev_i32_e32 v2, 9, v2
	v_add_u32_e32 v4, v2, v3
	v_mad_i32_i24 v2, v4, s4, v72
	v_mul_i32_i24_e32 v5, 0xffffdf00, v4
	v_cmp_lt_i32_e32 vcc, s5, v2
	s_and_saveexec_b64 s[0:1], vcc
	s_xor_b64 s[0:1], exec, s[0:1]
	v_lshl_add_u32 v2, v4, 8, v5
	v_add3_u32 v2, v72, v2, s12
	v_ashrrev_i32_e32 v3, 31, v2
	v_lshlrev_b64 v[2:3], 12, v[2:3]
	v_lshl_add_u64 v[2:3], s[56:57], 0, v[2:3]
	s_or_saveexec_b64 s[0:1], s[0:1]
	v_mov_b64_e32 v[110:111], 0x6000
	s_xor_b64 exec, exec, s[0:1]
	v_lshlrev_b32_e32 v2, 13, v4
	v_add3_u32 v2, v5, v2, v72
	v_ashrrev_i32_e32 v3, 31, v2
	v_lshlrev_b64 v[2:3], 12, v[2:3]
	v_mul_i32_i24_e32 v110, 0x1800, v4
	v_lshl_add_u64 v[2:3], s[52:53], 0, v[2:3]
	v_ashrrev_i32_e32 v111, 31, v110
	s_or_b64 exec, exec, s[0:1]
	v_lshl_add_u64 v[2:3], v[2:3], 0, v[66:67]
	global_load_dwordx4 v[62:65], v[2:3], off nt
	global_load_dwordx4 v[58:61], v[2:3], off offset:1024 nt
	global_load_dwordx4 v[54:57], v[2:3], off offset:2048 nt
	global_load_dwordx4 v[50:53], v[2:3], off offset:3072 nt
	v_add_u32_e32 v88, 1, v72
	v_mul_hi_i32 v2, v88, s13
	v_lshrrev_b32_e32 v3, 31, v2
	v_ashrrev_i32_e32 v2, 11, v2
	v_add_u32_e32 v4, v2, v3
	v_mad_i32_i24 v2, v4, s4, v88
	v_mul_i32_i24_e32 v5, 0xffffdf00, v4
	v_cmp_lt_i32_e32 vcc, s5, v2
	s_and_saveexec_b64 s[0:1], vcc
	s_xor_b64 s[0:1], exec, s[0:1]
	v_lshl_add_u32 v2, v4, 8, v5
	v_add3_u32 v2, v72, v2, s14
	v_ashrrev_i32_e32 v3, 31, v2
	v_lshlrev_b64 v[2:3], 12, v[2:3]
	v_lshl_add_u64 v[2:3], s[56:57], 0, v[2:3]
	s_or_saveexec_b64 s[0:1], s[0:1]
	v_mov_b64_e32 v[112:113], 0x6000
	s_xor_b64 exec, exec, s[0:1]
	v_lshl_add_u32 v2, v4, 13, v5
	v_add3_u32 v2, v72, v2, 1
	v_ashrrev_i32_e32 v3, 31, v2
	v_lshlrev_b64 v[2:3], 12, v[2:3]
	v_mul_i32_i24_e32 v112, 0x1800, v4
	v_lshl_add_u64 v[2:3], s[52:53], 0, v[2:3]
	v_ashrrev_i32_e32 v113, 31, v112
	s_or_b64 exec, exec, s[0:1]
	v_lshl_add_u64 v[2:3], v[2:3], 0, v[66:67]
	global_load_dwordx4 v[34:37], v[2:3], off nt
	global_load_dwordx4 v[30:33], v[2:3], off offset:1024 nt
	global_load_dwordx4 v[26:29], v[2:3], off offset:2048 nt
	global_load_dwordx4 v[22:25], v[2:3], off offset:3072 nt
	v_add_u32_e32 v86, 2, v72
	v_mul_hi_i32 v2, v86, s13
	v_lshrrev_b32_e32 v3, 31, v2
	v_ashrrev_i32_e32 v2, 11, v2
	v_add_u32_e32 v4, v2, v3
	v_mad_i32_i24 v2, v4, s4, v86
	v_mul_i32_i24_e32 v5, 0xffffdf00, v4
	v_cmp_lt_i32_e32 vcc, s5, v2
	s_and_saveexec_b64 s[0:1], vcc
	s_xor_b64 s[0:1], exec, s[0:1]
	v_lshl_add_u32 v2, v4, 8, v5
	v_add3_u32 v2, v72, v2, s15
	v_ashrrev_i32_e32 v3, 31, v2
	v_lshlrev_b64 v[2:3], 12, v[2:3]
	v_lshl_add_u64 v[2:3], s[56:57], 0, v[2:3]
	s_or_saveexec_b64 s[0:1], s[0:1]
	v_mov_b64_e32 v[96:97], 0x6000
	s_xor_b64 exec, exec, s[0:1]
	v_lshl_add_u32 v2, v4, 13, v5
	v_add3_u32 v2, v72, v2, 2
	v_ashrrev_i32_e32 v3, 31, v2
	v_lshlrev_b64 v[2:3], 12, v[2:3]
	v_mul_i32_i24_e32 v96, 0x1800, v4
	v_lshl_add_u64 v[2:3], s[52:53], 0, v[2:3]
	v_ashrrev_i32_e32 v97, 31, v96
	s_or_b64 exec, exec, s[0:1]
	v_lshl_add_u64 v[2:3], v[2:3], 0, v[66:67]
	global_load_dwordx4 v[14:17], v[2:3], off nt
	global_load_dwordx4 v[10:13], v[2:3], off offset:1024 nt
	global_load_dwordx4 v[6:9], v[2:3], off offset:2048 nt
	s_nop 0
	global_load_dwordx4 v[2:5], v[2:3], off offset:3072 nt
	v_lshl_add_u64 v[90:91], v[110:111], 2, s[26:27]
	s_waitcnt vmcnt(11)
	v_mul_f32_e32 v44, v63, v63
	s_waitcnt vmcnt(10)
	v_mul_f32_e32 v45, v59, v59
	s_waitcnt vmcnt(9)
	v_mul_f32_e32 v46, v55, v55
	v_fmac_f32_e32 v44, v62, v62
	v_fmac_f32_e32 v45, v58, v58
	v_lshl_add_u64 v[38:39], v[90:91], 0, s[10:11]
	s_waitcnt vmcnt(8)
	v_mul_f32_e32 v47, v51, v51
	v_fmac_f32_e32 v46, v54, v54
	v_lshl_add_u64 v[40:41], v[90:91], 0, v[66:67]
	v_fmac_f32_e32 v44, v64, v64
	v_fmac_f32_e32 v45, v60, v60
	v_lshl_add_u64 v[18:19], v[38:39], 0, v[76:77]
	v_lshl_add_u64 v[42:43], v[38:39], 0, v[80:81]
	global_load_dwordx4 v[98:101], v[68:69], off offset:3072 nt
	global_load_dwordx4 v[102:105], v[68:69], off offset:2048 nt
	global_load_dwordx4 v[106:109], v[68:69], off offset:1024 nt
	v_fmac_f32_e32 v47, v50, v50
	v_fmac_f32_e32 v46, v56, v56
	global_load_dwordx4 v[92:95], v[18:19], off nt
	s_nop 0
	global_load_dwordx4 v[18:21], v[40:41], off offset:3072 nt
	global_load_dwordx4 v[126:129], v[42:43], off nt
	v_lshl_add_u64 v[42:43], v[38:39], 0, v[84:85]
	v_lshl_add_u64 v[38:39], v[38:39], 0, v[66:67]
	v_fmac_f32_e32 v44, v65, v65
	v_fmac_f32_e32 v45, v61, v61
	v_fmac_f32_e32 v47, v52, v52
	global_load_dwordx4 v[130:133], v[42:43], off nt
	global_load_dwordx4 v[134:137], v[38:39], off nt
	v_fmac_f32_e32 v46, v57, v57
	v_add_f32_e32 v38, v44, v45
	v_fmac_f32_e32 v47, v53, v53
	v_add_f32_e32 v38, v38, v46
	s_waitcnt vmcnt(15)
	v_mul_f32_e32 v48, v35, v35
	s_waitcnt vmcnt(14)
	v_mul_f32_e32 v49, v31, v31
	v_add_f32_e32 v38, v38, v47
	s_waitcnt vmcnt(13)
	v_mul_f32_e32 v73, v27, v27
	v_fmac_f32_e32 v48, v34, v34
	v_fmac_f32_e32 v49, v30, v30
	ds_bpermute_b32 v39, v114, v38
	s_waitcnt vmcnt(12)
	v_mul_f32_e32 v75, v23, v23
	v_fmac_f32_e32 v73, v26, v26
	v_fmac_f32_e32 v48, v36, v36
	v_fmac_f32_e32 v49, v32, v32
	v_fmac_f32_e32 v75, v22, v22
	v_fmac_f32_e32 v73, v28, v28
	v_fmac_f32_e32 v48, v37, v37
	v_fmac_f32_e32 v49, v33, v33
	v_fmac_f32_e32 v75, v24, v24
	v_fmac_f32_e32 v73, v29, v29
	v_add_f32_e32 v42, v48, v49
	v_fmac_f32_e32 v75, v25, v25
	v_add_f32_e32 v42, v42, v73
	v_add_f32_e32 v46, v42, v75
	s_waitcnt lgkmcnt(0)
	v_add_f32_e32 v38, v38, v39
	ds_bpermute_b32 v47, v114, v46
	ds_bpermute_b32 v39, v115, v38
	global_load_dwordx4 v[138:141], v[68:69], off nt
	global_load_dwordx4 v[42:45], v[40:41], off nt
	s_waitcnt lgkmcnt(1)
; __device__ __forceinline__ int pack4_fp8(float a, float b, float c, float d) { int w = __builtin_amdgcn_cvt_pk_fp8_f32(a, b, 0, false); return __builtin_amdgcn_cvt_pk_fp8_f32(c, d, w, true); }
; __device__ void phase1a(const Params& p) {
;     ...
;         for (int o = 32; o >= 1; o >>= 1) { ss[0] += __shfl_xor(ss[0], o); ss[1] += __shfl_xor(ss[1], o); ss[2] += __shfl_xor(ss[2], o); }
; #pragma unroll
;         for (int j = 0; j < 3; ++j) {
;             const int R = R0 + j;
;             if (R < MR) {
;                 if (md[j] != mcur) {
;                     mcur = md[j];
; #pragma unroll
;                     for (int i = 0; i < 4; ++i) {
;                         const int k = i * 256 + lane * 4;
;                         const float4 n1 = *(const float4*)(p.norm1 + k), sh = *(const float4*)(mcur + k), sc = *(const float4*)(mcur + 1024 + k);
;                         mf[i] = make_float4(n1.x * (1.f + sc.x), n1.y * (1.f + sc.y), n1.z * (1.f + sc.z), n1.w * (1.f + sc.w)); ma[i] = sh;
;                     }
;                 }
;                 const float rstd = 1.0f / sqrtf(ss[j] * (1.0f / 1024.0f) + EPS);
; #pragma unroll
;                 for (int i = 0; i < 4; ++i) {
;                     const int k = i * 256 + lane * 4;
;                     f32x4 o;
;                     o[0] = (v[j][i].x * rstd) * mf[i].x + ma[i].x; o[1] = (v[j][i].y * rstd) * mf[i].y + ma[i].y;
;                     o[2] = (v[j][i].z * rstd) * mf[i].z + ma[i].z; o[3] = (v[j][i].w * rstd) * mf[i].w + ma[i].w;
;                     *(int*)(p.h8 + (size_t)R * D + k) = pack4_fp8(__builtin_amdgcn_fmed3f(o[0] * H8S, -440.f, 440.f), __builtin_amdgcn_fmed3f(o[1] * H8S, -440.f, 440.f), __builtin_amdgcn_fmed3f(o[2] * H8S, -440.f, 440.f), __builtin_amdgcn_fmed3f(o[3] * H8S, -440.f, 440.f));
;                 }
	v_add_f32_e32 v46, v46, v47
	s_waitcnt lgkmcnt(0)
	v_add_f32_e32 v38, v38, v39
	ds_bpermute_b32 v47, v115, v46
	ds_bpermute_b32 v39, v116, v38
	s_waitcnt lgkmcnt(1)
	v_add_f32_e32 v46, v46, v47
	s_waitcnt lgkmcnt(0)
	v_add_f32_e32 v38, v38, v39
	ds_bpermute_b32 v47, v116, v46
	ds_bpermute_b32 v39, v117, v38
	s_waitcnt lgkmcnt(1)
	v_add_f32_e32 v46, v46, v47
	s_waitcnt lgkmcnt(0)
	v_add_f32_e32 v38, v38, v39
	ds_bpermute_b32 v47, v117, v46
	ds_bpermute_b32 v39, v118, v38
	s_waitcnt vmcnt(13)
	v_mul_f32_e32 v48, v15, v15
	s_waitcnt vmcnt(12)
	v_mul_f32_e32 v49, v11, v11
	s_waitcnt vmcnt(11)
	v_mul_f32_e32 v73, v7, v7
	v_fmac_f32_e32 v48, v14, v14
	v_fmac_f32_e32 v49, v10, v10
	s_waitcnt vmcnt(10)
	v_mul_f32_e32 v75, v3, v3
	v_fmac_f32_e32 v73, v6, v6
	v_fmac_f32_e32 v48, v16, v16
	v_fmac_f32_e32 v49, v12, v12
	v_fmac_f32_e32 v75, v2, v2
	v_fmac_f32_e32 v73, v8, v8
	v_fmac_f32_e32 v48, v17, v17
	v_fmac_f32_e32 v49, v13, v13
	v_fmac_f32_e32 v75, v4, v4
	v_fmac_f32_e32 v73, v9, v9
	v_add_f32_e32 v48, v48, v49
	v_fmac_f32_e32 v75, v5, v5
	v_add_f32_e32 v48, v48, v73
	v_add_f32_e32 v48, v48, v75
	ds_bpermute_b32 v49, v114, v48
	s_waitcnt lgkmcnt(2)
	v_add_f32_e32 v73, v46, v47
	s_waitcnt lgkmcnt(1)
	v_add_f32_e32 v79, v38, v39
	ds_bpermute_b32 v75, v118, v73
	ds_bpermute_b32 v83, v119, v79
	s_waitcnt lgkmcnt(2)
	v_add_f32_e32 v48, v48, v49
	ds_bpermute_b32 v49, v115, v48
	s_waitcnt vmcnt(6)
	v_pk_add_f32 v[94:95], v[94:95], 1.0 op_sel_hi:[1,0]
	s_waitcnt lgkmcnt(2)
	v_add_f32_e32 v89, v73, v75
	s_waitcnt lgkmcnt(1)
	v_add_f32_e32 v73, v79, v83
	v_fmamk_f32 v73, v73, 0x3a800000, v120
	s_waitcnt lgkmcnt(0)
	v_add_f32_e32 v48, v48, v49
	ds_bpermute_b32 v49, v116, v48
	v_cmp_gt_f32_e32 vcc, s16, v73
	v_pk_add_f32 v[142:143], v[92:93], 1.0 op_sel_hi:[1,0]
	v_pk_mul_f32 v[92:93], v[100:101], v[94:95]
	s_waitcnt vmcnt(4)
	v_pk_add_f32 v[100:101], v[126:127], 1.0 op_sel_hi:[1,0]
	s_waitcnt lgkmcnt(0)
	v_add_f32_e32 v87, v48, v49
	global_load_dwordx4 v[46:49], v[40:41], off offset:1024 nt
	s_nop 0
	global_load_dwordx4 v[38:41], v[40:41], off offset:2048 nt
	ds_bpermute_b32 v123, v117, v87
	v_pk_mul_f32 v[94:95], v[98:99], v[142:143]
	v_pk_add_f32 v[98:99], v[128:129], 1.0 op_sel_hi:[1,0]
	v_pk_mul_f32 v[100:101], v[102:103], v[100:101]
	s_waitcnt vmcnt(5)
	v_pk_add_f32 v[102:103], v[132:133], 1.0 op_sel_hi:[1,0]
	s_waitcnt lgkmcnt(0)
	v_add_f32_e32 v75, v87, v123
	ds_bpermute_b32 v79, v118, v75
	v_pk_mul_f32 v[98:99], v[104:105], v[98:99]
	v_pk_mul_f32 v[102:103], v[108:109], v[102:103]
	v_pk_add_f32 v[104:105], v[130:131], 1.0 op_sel_hi:[1,0]
	s_waitcnt vmcnt(4)
	v_pk_add_f32 v[108:109], v[134:135], 1.0 op_sel_hi:[1,0]
	s_waitcnt lgkmcnt(0)
	v_add_f32_e32 v87, v75, v79
	v_mul_f32_e32 v75, 0x4f800000, v73
	v_cndmask_b32_e32 v73, v73, v75, vcc
	v_sqrt_f32_e32 v75, v73
	v_pk_mul_f32 v[104:105], v[106:107], v[104:105]
	v_pk_add_f32 v[106:107], v[136:137], 1.0 op_sel_hi:[1,0]
	ds_bpermute_b32 v124, v119, v89
	v_add_u32_e32 v79, -1, v75
	v_fma_f32 v83, -v79, v75, v73
	v_cmp_ge_f32_e64 s[0:1], 0, v83
	v_add_u32_e32 v83, 1, v75
	s_waitcnt vmcnt(3)
	v_pk_mul_f32 v[108:109], v[138:139], v[108:109]
	v_cndmask_b32_e64 v79, v75, v79, s[0:1]
	v_fma_f32 v75, -v83, v75, v73
	v_cmp_lt_f32_e64 s[0:1], 0, v75
	v_pk_mul_f32 v[106:107], v[140:141], v[106:107]
	ds_bpermute_b32 v123, v119, v87
	v_cndmask_b32_e64 v75, v79, v83, s[0:1]
	v_mul_f32_e32 v79, 0x37800000, v75
	v_cndmask_b32_e32 v75, v75, v79, vcc
	v_cmp_class_f32_e32 vcc, v73, v121
	s_nop 1
	v_cndmask_b32_e32 v73, v75, v73, vcc
	v_div_scale_f32 v75, s[0:1], v73, v73, 1.0
	v_rcp_f32_e32 v79, v75
	s_nop 0
	v_fma_f32 v83, -v75, v79, 1.0
	v_fmac_f32_e32 v79, v83, v79
	v_div_scale_f32 v83, vcc, 1.0, v73, 1.0
	v_mul_f32_e32 v125, v83, v79
	v_fma_f32 v126, -v75, v125, v83
	v_fmac_f32_e32 v125, v126, v79
	v_fma_f32 v75, -v75, v125, v83
	v_div_fmas_f32 v75, v75, v79, v125
	v_div_fixup_f32 v75, v75, v73, 1.0
	v_mul_f32_e32 v62, v62, v75
	v_mul_f32_e32 v63, v63, v75
	v_ashrrev_i32_e32 v73, 31, v72
	s_waitcnt vmcnt(2)
	v_fma_f32 v62, v62, v108, v42
	v_fma_f32 v63, v63, v109, v43
	v_mul_f32_e32 v64, v64, v75
	v_lshlrev_b64 v[126:127], 10, v[72:73]
	v_fma_f32 v64, v64, v106, v44
	v_mul_f32_e32 v65, v65, v75
	v_mov_b32_e32 v73, v45
	v_mul_f32_e32 v62, 0x41000000, v62
	v_mul_f32_e32 v63, 0x41000000, v63
	v_mul_f32_e32 v58, v58, v75
	v_mul_f32_e32 v59, v59, v75
	v_fmac_f32_e32 v73, v65, v107
	v_med3_f32 v62, v62, s17, v122
	v_med3_f32 v63, v63, s17, v122
	v_mul_f32_e32 v64, 0x41000000, v64
	v_mov_b32_e32 v65, 0
	v_cvt_pk_fp8_f32 v65, v62, v63
	v_med3_f32 v62, v64, s17, v122
	v_mul_f32_e32 v61, v61, v75
	v_mul_f32_e32 v60, v60, v75
	v_mul_f32_e32 v54, v54, v75
	v_mul_f32_e32 v55, v55, v75
	v_mul_f32_e32 v57, v57, v75
	v_mul_f32_e32 v56, v56, v75
	s_waitcnt vmcnt(1)
	v_fma_f32 v58, v58, v104, v46
	v_fma_f32 v59, v59, v105, v47
	v_mov_b32_e32 v64, v49
	v_mul_f32_e32 v58, 0x41000000, v58
	v_mul_f32_e32 v59, 0x41000000, v59
	v_fmac_f32_e32 v64, v61, v103
	v_med3_f32 v58, v58, s17, v122
	v_med3_f32 v59, v59, s17, v122
	v_mov_b32_e32 v61, 0
	v_cvt_pk_fp8_f32 v61, v58, v59
	v_fma_f32 v60, v60, v102, v48
	v_mul_f32_e32 v60, 0x41000000, v60
	v_mul_f32_e32 v59, 0x41000000, v64
	v_med3_f32 v58, v60, s17, v122
	v_med3_f32 v59, v59, s17, v122
	s_waitcnt vmcnt(0)
	v_fma_f32 v54, v54, v100, v38
	v_fma_f32 v55, v55, v101, v39
	v_cvt_pk_fp8_f32 v61, v58, v59 op_sel:[0,0,1]
	v_mov_b32_e32 v58, v41
	v_mul_f32_e32 v54, 0x41000000, v54
	v_mul_f32_e32 v55, 0x41000000, v55
	v_fmac_f32_e32 v58, v57, v99
	v_med3_f32 v54, v54, s17, v122
	v_med3_f32 v55, v55, s17, v122
	v_mov_b32_e32 v57, 0
	v_cvt_pk_fp8_f32 v57, v54, v55
	v_fma_f32 v56, v56, v98, v40
	v_mul_f32_e32 v56, 0x41000000, v56
	v_mul_f32_e32 v55, 0x41000000, v58
	v_mul_f32_e32 v50, v50, v75
	v_mul_f32_e32 v51, v51, v75
	v_med3_f32 v54, v56, s17, v122
	v_med3_f32 v55, v55, s17, v122
	v_fma_f32 v50, v50, v94, v18
	v_fma_f32 v51, v51, v95, v19
	v_cvt_pk_fp8_f32 v57, v54, v55 op_sel:[0,0,1]
	v_mul_f32_e32 v53, v53, v75
	v_mov_b32_e32 v54, v21
	v_mul_f32_e32 v50, 0x41000000, v50
	v_mul_f32_e32 v51, 0x41000000, v51
	v_mul_f32_e32 v63, 0x41000000, v73
	v_fmac_f32_e32 v54, v93, v53
	v_med3_f32 v50, v50, s17, v122
	v_med3_f32 v51, v51, s17, v122
	v_mov_b32_e32 v53, 0
	v_med3_f32 v63, v63, s17, v122
	v_mul_f32_e32 v52, v52, v75
	v_cvt_pk_fp8_f32 v53, v50, v51
	v_cvt_pk_fp8_f32 v65, v62, v63 op_sel:[0,0,1]
	v_fma_f32 v52, v52, v92, v20
	v_mul_f32_e32 v52, 0x41000000, v52
	v_mul_f32_e32 v51, 0x41000000, v54
	v_med3_f32 v50, v52, s17, v122
	v_med3_f32 v51, v51, s17, v122
	v_lshl_add_u64 v[62:63], v[70:71], 0, v[126:127]
	v_cvt_pk_fp8_f32 v53, v50, v51 op_sel:[0,0,1]
	v_cmp_ne_u64_e32 vcc, v[112:113], v[110:111]
	global_store_dword v[62:63], v65, off
	global_store_dword v[62:63], v61, off offset:256
	global_store_dword v[62:63], v57, off offset:512
	global_store_dword v[62:63], v53, off offset:768
	s_and_saveexec_b64 s[0:1], vcc
	s_cbranch_execz .LBB0_142
; __device__ void phase1a(const Params& p) {
;     ...
;                 if (md[j] != mcur) {
;                     mcur = md[j];
; #pragma unroll
;                     for (int i = 0; i < 4; ++i) {
;                         const int k = i * 256 + lane * 4;
;                         const float4 n1 = *(const float4*)(p.norm1 + k), sh = *(const float4*)(mcur + k), sc = *(const float4*)(mcur + 1024 + k);
;                         mf[i] = make_float4(n1.x * (1.f + sc.x), n1.y * (1.f + sc.y), n1.z * (1.f + sc.z), n1.w * (1.f + sc.w)); ma[i] = sh;
;                     }
	v_lshl_add_u64 v[90:91], v[112:113], 2, s[26:27]
	v_lshl_add_u64 v[18:19], v[90:91], 0, s[10:11]
	v_lshl_add_u64 v[20:21], v[18:19], 0, v[66:67]
	v_mov_b32_e32 v83, v67
	v_mov_b32_e32 v79, v67
	v_lshl_add_u64 v[38:39], v[18:19], 0, v[82:83]
	global_load_dwordx4 v[50:53], v[20:21], off nt
	global_load_dwordx4 v[54:57], v[38:39], off nt
	v_lshl_add_u64 v[20:21], v[18:19], 0, v[78:79]
	v_mov_b32_e32 v75, v67
	global_load_dwordx4 v[58:61], v[20:21], off nt
	v_lshl_add_u64 v[18:19], v[18:19], 0, v[74:75]
	global_load_dwordx4 v[62:65], v[18:19], off nt
	global_load_dwordx4 v[92:95], v[68:69], off nt
	v_lshl_add_u64 v[18:19], v[90:91], 0, v[66:67]
	global_load_dwordx4 v[98:101], v[68:69], off offset:1024 nt
	global_load_dwordx4 v[110:113], v[68:69], off offset:2048 nt
	global_load_dwordx4 v[42:45], v[18:19], off nt
	global_load_dwordx4 v[46:49], v[18:19], off offset:1024 nt
	global_load_dwordx4 v[126:129], v[68:69], off offset:3072 nt
	global_load_dwordx4 v[38:41], v[18:19], off offset:2048 nt
	s_nop 0
	global_load_dwordx4 v[18:21], v[18:19], off offset:3072 nt
	s_waitcnt vmcnt(11)
	v_pk_add_f32 v[50:51], v[50:51], 1.0 op_sel_hi:[1,0]
	v_pk_add_f32 v[52:53], v[52:53], 1.0 op_sel_hi:[1,0]
	s_waitcnt vmcnt(10)
	v_pk_add_f32 v[54:55], v[54:55], 1.0 op_sel_hi:[1,0]
	v_pk_add_f32 v[56:57], v[56:57], 1.0 op_sel_hi:[1,0]
	s_waitcnt vmcnt(9)
	v_pk_add_f32 v[58:59], v[58:59], 1.0 op_sel_hi:[1,0]
	v_pk_add_f32 v[60:61], v[60:61], 1.0 op_sel_hi:[1,0]
	s_waitcnt vmcnt(8)
	v_pk_add_f32 v[62:63], v[62:63], 1.0 op_sel_hi:[1,0]
	v_pk_add_f32 v[64:65], v[64:65], 1.0 op_sel_hi:[1,0]
	s_waitcnt vmcnt(7)
	v_pk_mul_f32 v[108:109], v[92:93], v[50:51]
	v_pk_mul_f32 v[106:107], v[94:95], v[52:53]
	s_waitcnt vmcnt(6)
	v_pk_mul_f32 v[104:105], v[98:99], v[54:55]
	v_pk_mul_f32 v[102:103], v[100:101], v[56:57]
	s_waitcnt vmcnt(5)
	v_pk_mul_f32 v[100:101], v[110:111], v[58:59]
	v_pk_mul_f32 v[98:99], v[112:113], v[60:61]
	s_waitcnt vmcnt(2)
	v_pk_mul_f32 v[94:95], v[126:127], v[62:63]
	v_pk_mul_f32 v[92:93], v[128:129], v[64:65]
; __device__ __forceinline__ int pack4_fp8(float a, float b, float c, float d) { int w = __builtin_amdgcn_cvt_pk_fp8_f32(a, b, 0, false); return __builtin_amdgcn_cvt_pk_fp8_f32(c, d, w, true); }
; __device__ void phase1a(const Params& p) {
;     ...
;                 if (md[j] != mcur) {
;                     mcur = md[j];
; #pragma unroll
;                     for (int i = 0; i < 4; ++i) {
;                         const int k = i * 256 + lane * 4;
;                         const float4 n1 = *(const float4*)(p.norm1 + k), sh = *(const float4*)(mcur + k), sc = *(const float4*)(mcur + 1024 + k);
;                         mf[i] = make_float4(n1.x * (1.f + sc.x), n1.y * (1.f + sc.y), n1.z * (1.f + sc.z), n1.w * (1.f + sc.w)); ma[i] = sh;
;                     }
;     ...
;                 const float rstd = 1.0f / sqrtf(ss[j] * (1.0f / 1024.0f) + EPS);
; #pragma unroll
;                 for (int i = 0; i < 4; ++i) {
;                     const int k = i * 256 + lane * 4;
;                     f32x4 o;
;                     o[0] = (v[j][i].x * rstd) * mf[i].x + ma[i].x; o[1] = (v[j][i].y * rstd) * mf[i].y + ma[i].y;
;                     o[2] = (v[j][i].z * rstd) * mf[i].z + ma[i].z; o[3] = (v[j][i].w * rstd) * mf[i].w + ma[i].w;
;                     *(int*)(p.h8 + (size_t)R * D + k) = pack4_fp8(__builtin_amdgcn_fmed3f(o[0] * H8S, -440.f, 440.f), __builtin_amdgcn_fmed3f(o[1] * H8S, -440.f, 440.f), __builtin_amdgcn_fmed3f(o[2] * H8S, -440.f, 440.f), __builtin_amdgcn_fmed3f(o[3] * H8S, -440.f, 440.f));
;                 }
.LBB0_142:
	s_or_b64 exec, exec, s[0:1]
	s_waitcnt lgkmcnt(1)
	v_add_f32_e32 v50, v89, v124
	v_fmamk_f32 v50, v50, 0x3a800000, v120
	v_mul_f32_e32 v51, 0x4f800000, v50
	v_cmp_gt_f32_e32 vcc, s16, v50
	v_ashrrev_i32_e32 v89, 31, v88
	s_nop 0
	v_cndmask_b32_e32 v50, v50, v51, vcc
	v_sqrt_f32_e32 v51, v50
	s_nop 0
	v_add_u32_e32 v52, -1, v51
	v_fma_f32 v54, -v52, v51, v50
	v_add_u32_e32 v53, 1, v51
	v_cmp_ge_f32_e64 s[0:1], 0, v54
	s_nop 1
	v_cndmask_b32_e64 v52, v51, v52, s[0:1]
	v_fma_f32 v51, -v53, v51, v50
	v_cmp_lt_f32_e64 s[0:1], 0, v51
	s_nop 1
	v_cndmask_b32_e64 v51, v52, v53, s[0:1]
	v_mul_f32_e32 v52, 0x37800000, v51
	v_cndmask_b32_e32 v51, v51, v52, vcc
	v_cmp_class_f32_e32 vcc, v50, v121
	s_nop 1
	v_cndmask_b32_e32 v52, v51, v50, vcc
	v_div_scale_f32 v53, s[0:1], v52, v52, 1.0
	v_rcp_f32_e32 v54, v53
	v_lshl_add_u64 v[50:51], v[96:97], 2, s[26:27]
	v_fma_f32 v55, -v53, v54, 1.0
	v_fmac_f32_e32 v54, v55, v54
	v_div_scale_f32 v55, vcc, 1.0, v52, 1.0
	v_mul_f32_e32 v56, v55, v54
	v_fma_f32 v57, -v53, v56, v55
	v_fmac_f32_e32 v56, v57, v54
	v_fma_f32 v53, -v53, v56, v55
	v_div_fmas_f32 v53, v53, v54, v56
	v_div_fixup_f32 v54, v53, v52, 1.0
	v_mul_f32_e32 v34, v34, v54
	v_mul_f32_e32 v35, v35, v54
	v_fma_f32 v34, v34, v108, v42
	v_fma_f32 v35, v35, v109, v43
	v_mul_f32_e32 v36, v36, v54
	v_mul_f32_e32 v30, v30, v54
	v_mul_f32_e32 v31, v31, v54
	v_fma_f32 v36, v36, v106, v44
	v_mul_f32_e32 v34, 0x41000000, v34
	v_mul_f32_e32 v35, 0x41000000, v35
	v_fma_f32 v30, v30, v104, v46
	v_fma_f32 v31, v31, v105, v47
	v_med3_f32 v34, v34, s17, v122
	v_med3_f32 v35, v35, s17, v122
	v_mul_f32_e32 v36, 0x41000000, v36
	v_mov_b32_e32 v55, 0
	v_mul_f32_e32 v30, 0x41000000, v30
	v_mul_f32_e32 v31, 0x41000000, v31
	v_cvt_pk_fp8_f32 v55, v34, v35
	v_med3_f32 v34, v36, s17, v122
	v_med3_f32 v30, v30, s17, v122
	v_med3_f32 v31, v31, s17, v122
	v_mov_b32_e32 v36, 0
	v_mul_f32_e32 v32, v32, v54
	v_mul_f32_e32 v33, v33, v54
	v_cvt_pk_fp8_f32 v36, v30, v31
	v_fma_f32 v32, v32, v102, v48
	v_fma_f32 v33, v33, v103, v49
	v_mul_f32_e32 v26, v26, v54
	v_mul_f32_e32 v27, v27, v54
	v_mul_f32_e32 v32, 0x41000000, v32
	v_mul_f32_e32 v31, 0x41000000, v33
	s_waitcnt vmcnt(1)
	v_fma_f32 v26, v26, v100, v38
	v_fma_f32 v27, v27, v101, v39
	v_med3_f32 v30, v32, s17, v122
	v_med3_f32 v31, v31, s17, v122
	v_mul_f32_e32 v26, 0x41000000, v26
	v_mul_f32_e32 v27, 0x41000000, v27
	v_cvt_pk_fp8_f32 v36, v30, v31 op_sel:[0,0,1]
	v_med3_f32 v26, v26, s17, v122
	v_med3_f32 v27, v27, s17, v122
	v_mov_b32_e32 v30, 0
	v_mul_f32_e32 v28, v28, v54
	v_mul_f32_e32 v29, v29, v54
	v_cvt_pk_fp8_f32 v30, v26, v27
	v_fma_f32 v28, v28, v98, v40
	v_fma_f32 v29, v29, v99, v41
	v_mul_f32_e32 v22, v22, v54
	v_mul_f32_e32 v23, v23, v54
	v_mul_f32_e32 v37, v37, v54
	v_mul_f32_e32 v28, 0x41000000, v28
	v_mul_f32_e32 v27, 0x41000000, v29
	s_waitcnt vmcnt(0)
	v_fma_f32 v22, v22, v94, v18
	v_fma_f32 v23, v23, v95, v19
	v_fma_f32 v37, v37, v107, v45
	v_med3_f32 v26, v28, s17, v122
	v_med3_f32 v27, v27, s17, v122
	v_mul_f32_e32 v22, 0x41000000, v22
	v_mul_f32_e32 v23, 0x41000000, v23
	v_mul_f32_e32 v35, 0x41000000, v37
	v_cvt_pk_fp8_f32 v30, v26, v27 op_sel:[0,0,1]
	v_med3_f32 v22, v22, s17, v122
	v_med3_f32 v23, v23, s17, v122
	v_mov_b32_e32 v26, 0
	v_med3_f32 v35, v35, s17, v122
	v_mul_f32_e32 v24, v24, v54
	v_mul_f32_e32 v25, v25, v54
	v_cvt_pk_fp8_f32 v26, v22, v23
	v_cvt_pk_fp8_f32 v55, v34, v35 op_sel:[0,0,1]
	v_fma_f32 v24, v24, v92, v20
	v_fma_f32 v25, v25, v93, v21
	v_mul_f32_e32 v24, 0x41000000, v24
	v_mul_f32_e32 v23, 0x41000000, v25
	v_lshlrev_b64 v[52:53], 10, v[88:89]
	v_med3_f32 v22, v24, s17, v122
	v_med3_f32 v23, v23, s17, v122
	v_lshl_add_u64 v[34:35], v[70:71], 0, v[52:53]
	v_cvt_pk_fp8_f32 v26, v22, v23 op_sel:[0,0,1]
	v_cmp_ne_u64_e32 vcc, v[50:51], v[90:91]
	global_store_dword v[34:35], v55, off
	global_store_dword v[34:35], v36, off offset:256
	global_store_dword v[34:35], v30, off offset:512
	global_store_dword v[34:35], v26, off offset:768
	s_and_saveexec_b64 s[0:1], vcc
	s_cbranch_execz .LBB0_127
	v_lshl_add_u64 v[18:19], v[50:51], 0, s[10:11]
	v_mov_b32_e32 v83, v67
	v_lshl_add_u64 v[20:21], v[18:19], 0, v[66:67]
	v_lshl_add_u64 v[26:27], v[18:19], 0, v[82:83]
	v_mov_b32_e32 v79, v67
	global_load_dwordx4 v[22:25], v[20:21], off nt
	s_nop 0
	global_load_dwordx4 v[26:29], v[26:27], off nt
	v_lshl_add_u64 v[20:21], v[18:19], 0, v[78:79]
	v_mov_b32_e32 v75, v67
	global_load_dwordx4 v[30:33], v[20:21], off nt
	v_lshl_add_u64 v[18:19], v[18:19], 0, v[74:75]
	global_load_dwordx4 v[34:37], v[18:19], off nt
	global_load_dwordx4 v[52:55], v[68:69], off nt
	v_lshl_add_u64 v[18:19], v[50:51], 0, v[66:67]
	global_load_dwordx4 v[56:59], v[68:69], off offset:1024 nt
	global_load_dwordx4 v[60:63], v[68:69], off offset:2048 nt
	global_load_dwordx4 v[42:45], v[18:19], off nt
	global_load_dwordx4 v[46:49], v[18:19], off offset:1024 nt
	global_load_dwordx4 v[88:91], v[68:69], off offset:3072 nt
	global_load_dwordx4 v[38:41], v[18:19], off offset:2048 nt
	s_nop 0
	global_load_dwordx4 v[18:21], v[18:19], off offset:3072 nt
	s_waitcnt vmcnt(11)
	v_pk_add_f32 v[22:23], v[22:23], 1.0 op_sel_hi:[1,0]
	v_pk_add_f32 v[24:25], v[24:25], 1.0 op_sel_hi:[1,0]
	s_waitcnt vmcnt(10)
	v_pk_add_f32 v[26:27], v[26:27], 1.0 op_sel_hi:[1,0]
	v_pk_add_f32 v[28:29], v[28:29], 1.0 op_sel_hi:[1,0]
	s_waitcnt vmcnt(9)
	v_pk_add_f32 v[30:31], v[30:31], 1.0 op_sel_hi:[1,0]
	v_pk_add_f32 v[32:33], v[32:33], 1.0 op_sel_hi:[1,0]
	s_waitcnt vmcnt(8)
	v_pk_add_f32 v[34:35], v[34:35], 1.0 op_sel_hi:[1,0]
	v_pk_add_f32 v[36:37], v[36:37], 1.0 op_sel_hi:[1,0]
	s_waitcnt vmcnt(7)
	v_pk_mul_f32 v[108:109], v[52:53], v[22:23]
	v_pk_mul_f32 v[106:107], v[54:55], v[24:25]
	s_waitcnt vmcnt(6)
	v_pk_mul_f32 v[104:105], v[56:57], v[26:27]
	v_pk_mul_f32 v[102:103], v[58:59], v[28:29]
	s_waitcnt vmcnt(5)
	v_pk_mul_f32 v[100:101], v[60:61], v[30:31]
	v_pk_mul_f32 v[98:99], v[62:63], v[32:33]
	s_waitcnt vmcnt(2)
	v_pk_mul_f32 v[94:95], v[88:89], v[34:35]
	v_pk_mul_f32 v[92:93], v[90:91], v[36:37]
	s_branch .LBB0_127

; __device__ __forceinline__ int pack4_fp8(float a, float b, float c, float d) { int w = __builtin_amdgcn_cvt_pk_fp8_f32(a, b, 0, false); return __builtin_amdgcn_cvt_pk_fp8_f32(c, d, w, true); }
; __device__ void rt5b_stream(const Params& p, unsigned char* smem, const XMap& xm) {
;     ...
;                 if (wact) {
;                     unsigned char* stg = smem + 65536 + 32768 + wid * STG_WAVE;
;                     unsigned char* ybase = p.y + (j >> 1) * 256 + wc * 64;
; #pragma unroll
;                     for (int ps = 0; ps < 4; ++ps) {
;                         const int sl[2] = {ps == 0 ? sl00 : ps == 1 ? sl10 : ps == 2 ? sl20 : sl30, ps == 0 ? sl01 : ps == 1 ? sl11 : ps == 2 ? sl21 : sl31};
; #pragma unroll
;                         for (int mm = 0; mm < 2; ++mm)
; #pragma unroll
;                             for (int n = 0; n < 4; ++n) {
;                                 const f32x4 v = acc[ps * 2 + mm][n] * (16.0f / (A8S * D8S));
;                                 *(int*)(stg + (mm * 16 + l15) * 68 + n * 16 + gq * 4) = pack4_fp8(__builtin_amdgcn_fmed3f(v[0], -440.f, 440.f), __builtin_amdgcn_fmed3f(v[1], -440.f, 440.f), __builtin_amdgcn_fmed3f(v[2], -440.f, 440.f), __builtin_amdgcn_fmed3f(v[3], -440.f, 440.f));
;                             }
;                         asm volatile("s_waitcnt lgkmcnt(0)" ::: "memory");
; #pragma unroll
;                         for (int i2 = 0; i2 < 2; ++i2) {
;                             const int row = i2 * 16 + (lane >> 2), ch = lane & 3;
;                             const unsigned char* q = stg + row * 68 + ch * 16;
;                             uint4 w; w.x = *(const unsigned*)(q); w.y = *(const unsigned*)(q + 4); w.z = *(const unsigned*)(q + 8); w.w = *(const unsigned*)(q + 12);
;                             if (sl[i2] >= 0) *(uint4*)(ybase + (size_t)sl[i2] * D + ch * 16) = w;
;                         }
;                         asm volatile("s_waitcnt lgkmcnt(0)" ::: "memory");
;                     }
.LBB0_1197:
	s_and_b64 vcc, exec, s[22:23]
	s_cbranch_vccnz .LBB0_1181
	v_pk_mul_f32 v[126:127], v[126:127], s[48:49] op_sel_hi:[1,0]
	v_mov_b32_e32 v130, 0
	v_med3_f32 v126, v126, s72, v180
	v_med3_f32 v127, v127, s72, v180
	v_cvt_pk_fp8_f32 v130, v126, v127
	v_pk_mul_f32 v[126:127], v[128:129], s[48:49] op_sel_hi:[1,0]
	v_pk_mul_f32 v[122:123], v[122:123], s[48:49] op_sel_hi:[1,0]
	v_med3_f32 v126, v126, s72, v180
	v_med3_f32 v127, v127, s72, v180
	v_cvt_pk_fp8_f32 v130, v126, v127 op_sel:[0,0,1]
	v_med3_f32 v122, v122, s72, v180
	v_med3_f32 v123, v123, s72, v180
	v_mov_b32_e32 v126, 0
	v_pk_mul_f32 v[118:119], v[118:119], s[48:49] op_sel_hi:[1,0]
	v_cvt_pk_fp8_f32 v126, v122, v123
	v_pk_mul_f32 v[122:123], v[124:125], s[48:49] op_sel_hi:[1,0]
	v_med3_f32 v118, v118, s72, v180
	v_med3_f32 v119, v119, s72, v180
	v_mov_b32_e32 v124, 0
	v_cvt_pk_fp8_f32 v124, v118, v119
	v_pk_mul_f32 v[118:119], v[120:121], s[48:49] op_sel_hi:[1,0]
	v_pk_mul_f32 v[114:115], v[114:115], s[48:49] op_sel_hi:[1,0]
	v_med3_f32 v118, v118, s72, v180
	v_med3_f32 v119, v119, s72, v180
	v_cvt_pk_fp8_f32 v124, v118, v119 op_sel:[0,0,1]
	v_med3_f32 v114, v114, s72, v180
	v_med3_f32 v115, v115, s72, v180
	v_mov_b32_e32 v118, 0
	v_cvt_pk_fp8_f32 v118, v114, v115
	v_pk_mul_f32 v[114:115], v[116:117], s[48:49] op_sel_hi:[1,0]
	v_pk_mul_f32 v[110:111], v[110:111], s[48:49] op_sel_hi:[1,0]
	v_med3_f32 v114, v114, s72, v180
	v_med3_f32 v115, v115, s72, v180
	v_cvt_pk_fp8_f32 v118, v114, v115 op_sel:[0,0,1]
	v_med3_f32 v110, v110, s72, v180
	v_med3_f32 v111, v111, s72, v180
	v_mov_b32_e32 v114, 0
	v_cvt_pk_fp8_f32 v114, v110, v111
	v_pk_mul_f32 v[110:111], v[112:113], s[48:49] op_sel_hi:[1,0]
	v_pk_mul_f32 v[106:107], v[106:107], s[48:49] op_sel_hi:[1,0]
	v_med3_f32 v110, v110, s72, v180
	v_med3_f32 v111, v111, s72, v180
	v_cvt_pk_fp8_f32 v114, v110, v111 op_sel:[0,0,1]
	v_med3_f32 v106, v106, s72, v180
	v_med3_f32 v107, v107, s72, v180
	v_mov_b32_e32 v110, 0
	v_cvt_pk_fp8_f32 v110, v106, v107
	v_pk_mul_f32 v[106:107], v[108:109], s[48:49] op_sel_hi:[1,0]
	v_pk_mul_f32 v[102:103], v[102:103], s[48:49] op_sel_hi:[1,0]
	v_med3_f32 v106, v106, s72, v180
	v_med3_f32 v107, v107, s72, v180
	v_cvt_pk_fp8_f32 v110, v106, v107 op_sel:[0,0,1]
	v_med3_f32 v102, v102, s72, v180
	v_med3_f32 v103, v103, s72, v180
	v_mov_b32_e32 v106, 0
	v_cvt_pk_fp8_f32 v106, v102, v103
	v_pk_mul_f32 v[102:103], v[104:105], s[48:49] op_sel_hi:[1,0]
	v_pk_mul_f32 v[98:99], v[98:99], s[48:49] op_sel_hi:[1,0]
	v_med3_f32 v102, v102, s72, v180
	v_med3_f32 v103, v103, s72, v180
	v_cvt_pk_fp8_f32 v106, v102, v103 op_sel:[0,0,1]
	v_med3_f32 v98, v98, s72, v180
	v_med3_f32 v99, v99, s72, v180
	v_mov_b32_e32 v102, 0
	v_cvt_pk_fp8_f32 v102, v98, v99
	v_med3_f32 v122, v122, s72, v180
	v_med3_f32 v123, v123, s72, v180
	v_pk_mul_f32 v[98:99], v[100:101], s[48:49] op_sel_hi:[1,0]
	v_cvt_pk_fp8_f32 v126, v122, v123 op_sel:[0,0,1]
	v_med3_f32 v98, v98, s72, v180
	v_med3_f32 v99, v99, s72, v180
	v_cvt_pk_fp8_f32 v102, v98, v99 op_sel:[0,0,1]
	v_add_u32_e32 v100, 0x400, v181
	ds_write2_b32 v181, v130, v126 offset1:4
	ds_write2_b32 v181, v124, v118 offset0:8 offset1:12
	ds_write2_b32 v100, v114, v110 offset0:16 offset1:20
	ds_write2_b32 v100, v106, v102 offset0:24 offset1:28
	s_waitcnt lgkmcnt(0)
	s_and_b32 s46, s77, 0x300
	v_lshl_add_u64 v[122:123], v[146:147], 0, s[46:47]
	s_and_saveexec_b64 s[22:23], s[6:7]
	s_cbranch_execz .LBB0_1200
	ds_read2_b32 v[102:103], v182 offset1:1
	ds_read2_b32 v[104:105], v182 offset0:2 offset1:3
	v_lshl_add_u64 v[98:99], v[122:123], 0, v[152:153]
	s_waitcnt lgkmcnt(0)
	global_store_dwordx4 v[98:99], v[102:105], off nt
.LBB0_1200:
	s_or_b64 exec, exec, s[22:23]
	v_add_u32_e32 v98, 0x440, v182
	v_add_u32_e32 v99, 0x448, v182
	s_and_saveexec_b64 s[22:23], s[8:9]
	s_cbranch_execz .LBB0_1202
	ds_read2_b32 v[102:103], v98 offset1:1
	ds_read2_b32 v[104:105], v99 offset1:1
	v_lshl_add_u64 v[106:107], v[122:123], 0, v[154:155]
	s_waitcnt lgkmcnt(0)
	global_store_dwordx4 v[106:107], v[102:105], off nt
.LBB0_1202:
	s_or_b64 exec, exec, s[22:23]
	v_pk_mul_f32 v[94:95], v[94:95], s[48:49] op_sel_hi:[1,0]
	v_mov_b32_e32 v101, 0
	v_med3_f32 v94, v94, s72, v180
	v_med3_f32 v95, v95, s72, v180
	v_cvt_pk_fp8_f32 v101, v94, v95
	v_pk_mul_f32 v[94:95], v[96:97], s[48:49] op_sel_hi:[1,0]
	v_pk_mul_f32 v[90:91], v[90:91], s[48:49] op_sel_hi:[1,0]
	v_med3_f32 v94, v94, s72, v180
	v_med3_f32 v95, v95, s72, v180
	v_cvt_pk_fp8_f32 v101, v94, v95 op_sel:[0,0,1]
	v_med3_f32 v90, v90, s72, v180
	v_med3_f32 v91, v91, s72, v180
	v_mov_b32_e32 v94, 0
	v_cvt_pk_fp8_f32 v94, v90, v91
	v_pk_mul_f32 v[90:91], v[92:93], s[48:49] op_sel_hi:[1,0]
	v_pk_mul_f32 v[86:87], v[86:87], s[48:49] op_sel_hi:[1,0]
	v_med3_f32 v90, v90, s72, v180
	v_med3_f32 v91, v91, s72, v180
	v_cvt_pk_fp8_f32 v94, v90, v91 op_sel:[0,0,1]
	v_med3_f32 v86, v86, s72, v180
	v_med3_f32 v87, v87, s72, v180
	v_mov_b32_e32 v90, 0
	v_cvt_pk_fp8_f32 v90, v86, v87
	v_pk_mul_f32 v[86:87], v[88:89], s[48:49] op_sel_hi:[1,0]
	v_pk_mul_f32 v[82:83], v[82:83], s[48:49] op_sel_hi:[1,0]
	v_med3_f32 v86, v86, s72, v180
	v_med3_f32 v87, v87, s72, v180
	v_cvt_pk_fp8_f32 v90, v86, v87 op_sel:[0,0,1]
	v_med3_f32 v82, v82, s72, v180
	v_med3_f32 v83, v83, s72, v180
	v_mov_b32_e32 v86, 0
	v_cvt_pk_fp8_f32 v86, v82, v83
	v_pk_mul_f32 v[82:83], v[84:85], s[48:49] op_sel_hi:[1,0]
	v_pk_mul_f32 v[78:79], v[78:79], s[48:49] op_sel_hi:[1,0]
	v_med3_f32 v82, v82, s72, v180
	v_med3_f32 v83, v83, s72, v180
	v_cvt_pk_fp8_f32 v86, v82, v83 op_sel:[0,0,1]
	v_med3_f32 v78, v78, s72, v180
	v_med3_f32 v79, v79, s72, v180
	v_mov_b32_e32 v82, 0
	v_cvt_pk_fp8_f32 v82, v78, v79
	v_pk_mul_f32 v[78:79], v[80:81], s[48:49] op_sel_hi:[1,0]
	v_pk_mul_f32 v[74:75], v[74:75], s[48:49] op_sel_hi:[1,0]
	v_med3_f32 v78, v78, s72, v180
	v_med3_f32 v79, v79, s72, v180
	v_cvt_pk_fp8_f32 v82, v78, v79 op_sel:[0,0,1]
	v_med3_f32 v74, v74, s72, v180
	v_med3_f32 v75, v75, s72, v180
	v_mov_b32_e32 v78, 0
	v_cvt_pk_fp8_f32 v78, v74, v75
	v_pk_mul_f32 v[74:75], v[76:77], s[48:49] op_sel_hi:[1,0]
	v_pk_mul_f32 v[70:71], v[70:71], s[48:49] op_sel_hi:[1,0]
	v_med3_f32 v74, v74, s72, v180
	v_med3_f32 v75, v75, s72, v180
	v_cvt_pk_fp8_f32 v78, v74, v75 op_sel:[0,0,1]
	v_med3_f32 v70, v70, s72, v180
	v_med3_f32 v71, v71, s72, v180
	v_mov_b32_e32 v74, 0
	v_cvt_pk_fp8_f32 v74, v70, v71
	v_pk_mul_f32 v[70:71], v[72:73], s[48:49] op_sel_hi:[1,0]
	v_pk_mul_f32 v[66:67], v[66:67], s[48:49] op_sel_hi:[1,0]
	v_med3_f32 v70, v70, s72, v180
	v_med3_f32 v71, v71, s72, v180
	v_cvt_pk_fp8_f32 v74, v70, v71 op_sel:[0,0,1]
	v_med3_f32 v66, v66, s72, v180
	v_med3_f32 v67, v67, s72, v180
	v_mov_b32_e32 v70, 0
	v_cvt_pk_fp8_f32 v70, v66, v67
	v_pk_mul_f32 v[66:67], v[68:69], s[48:49] op_sel_hi:[1,0]
	s_waitcnt lgkmcnt(0)
; __device__ __forceinline__ int pack4_fp8(float a, float b, float c, float d) { int w = __builtin_amdgcn_cvt_pk_fp8_f32(a, b, 0, false); return __builtin_amdgcn_cvt_pk_fp8_f32(c, d, w, true); }
; __device__ void rt5b_stream(const Params& p, unsigned char* smem, const XMap& xm) {
;     ...
;                 if (wact) {
;                     unsigned char* stg = smem + 65536 + 32768 + wid * STG_WAVE;
;                     unsigned char* ybase = p.y + (j >> 1) * 256 + wc * 64;
; #pragma unroll
;                     for (int ps = 0; ps < 4; ++ps) {
;                         const int sl[2] = {ps == 0 ? sl00 : ps == 1 ? sl10 : ps == 2 ? sl20 : sl30, ps == 0 ? sl01 : ps == 1 ? sl11 : ps == 2 ? sl21 : sl31};
; #pragma unroll
;                         for (int mm = 0; mm < 2; ++mm)
; #pragma unroll
;                             for (int n = 0; n < 4; ++n) {
;                                 const f32x4 v = acc[ps * 2 + mm][n] * (16.0f / (A8S * D8S));
;                                 *(int*)(stg + (mm * 16 + l15) * 68 + n * 16 + gq * 4) = pack4_fp8(__builtin_amdgcn_fmed3f(v[0], -440.f, 440.f), __builtin_amdgcn_fmed3f(v[1], -440.f, 440.f), __builtin_amdgcn_fmed3f(v[2], -440.f, 440.f), __builtin_amdgcn_fmed3f(v[3], -440.f, 440.f));
;                             }
;                         asm volatile("s_waitcnt lgkmcnt(0)" ::: "memory");
; #pragma unroll
;                         for (int i2 = 0; i2 < 2; ++i2) {
;                             const int row = i2 * 16 + (lane >> 2), ch = lane & 3;
;                             const unsigned char* q = stg + row * 68 + ch * 16;
;                             uint4 w; w.x = *(const unsigned*)(q); w.y = *(const unsigned*)(q + 4); w.z = *(const unsigned*)(q + 8); w.w = *(const unsigned*)(q + 12);
;                             if (sl[i2] >= 0) *(uint4*)(ybase + (size_t)sl[i2] * D + ch * 16) = w;
;                         }
;                         asm volatile("s_waitcnt lgkmcnt(0)" ::: "memory");
;                     }
	s_nop 0
	v_med3_f32 v66, v66, s72, v180
	v_med3_f32 v67, v67, s72, v180
	v_cvt_pk_fp8_f32 v70, v66, v67 op_sel:[0,0,1]
	ds_write2_b32 v181, v101, v94 offset1:4
	ds_write2_b32 v181, v90, v86 offset0:8 offset1:12
	ds_write2_b32 v100, v82, v78 offset0:16 offset1:20
	ds_write2_b32 v100, v74, v70 offset0:24 offset1:28
	s_waitcnt lgkmcnt(0)
	s_and_saveexec_b64 s[22:23], s[10:11]
	s_cbranch_execz .LBB0_1204
	ds_read2_b32 v[66:67], v182 offset1:1
	ds_read2_b32 v[68:69], v182 offset0:2 offset1:3
	v_lshl_add_u64 v[70:71], v[122:123], 0, v[156:157]
	s_waitcnt lgkmcnt(0)
	global_store_dwordx4 v[70:71], v[66:69], off nt
.LBB0_1204:
	s_or_b64 exec, exec, s[22:23]
	s_and_saveexec_b64 s[22:23], s[12:13]
	s_cbranch_execz .LBB0_1206
	ds_read2_b32 v[66:67], v98 offset1:1
	ds_read2_b32 v[68:69], v99 offset1:1
	v_lshl_add_u64 v[70:71], v[122:123], 0, v[158:159]
	s_waitcnt lgkmcnt(0)
	global_store_dwordx4 v[70:71], v[66:69], off nt
.LBB0_1206:
	s_or_b64 exec, exec, s[22:23]
	v_pk_mul_f32 v[62:63], v[62:63], s[48:49] op_sel_hi:[1,0]
	v_mov_b32_e32 v66, 0
	v_med3_f32 v62, v62, s72, v180
	v_med3_f32 v63, v63, s72, v180
	v_cvt_pk_fp8_f32 v66, v62, v63
	v_pk_mul_f32 v[62:63], v[64:65], s[48:49] op_sel_hi:[1,0]
	v_pk_mul_f32 v[58:59], v[58:59], s[48:49] op_sel_hi:[1,0]
	v_med3_f32 v62, v62, s72, v180
	v_med3_f32 v63, v63, s72, v180
	v_cvt_pk_fp8_f32 v66, v62, v63 op_sel:[0,0,1]
	v_med3_f32 v58, v58, s72, v180
	v_med3_f32 v59, v59, s72, v180
	v_mov_b32_e32 v62, 0
	v_cvt_pk_fp8_f32 v62, v58, v59
	v_pk_mul_f32 v[58:59], v[60:61], s[48:49] op_sel_hi:[1,0]
	v_pk_mul_f32 v[54:55], v[54:55], s[48:49] op_sel_hi:[1,0]
	v_med3_f32 v58, v58, s72, v180
	v_med3_f32 v59, v59, s72, v180
	v_cvt_pk_fp8_f32 v62, v58, v59 op_sel:[0,0,1]
	v_med3_f32 v54, v54, s72, v180
	v_med3_f32 v55, v55, s72, v180
	v_mov_b32_e32 v58, 0
	v_cvt_pk_fp8_f32 v58, v54, v55
	v_pk_mul_f32 v[54:55], v[56:57], s[48:49] op_sel_hi:[1,0]
	v_pk_mul_f32 v[50:51], v[50:51], s[48:49] op_sel_hi:[1,0]
	v_med3_f32 v54, v54, s72, v180
	v_med3_f32 v55, v55, s72, v180
	v_cvt_pk_fp8_f32 v58, v54, v55 op_sel:[0,0,1]
	v_med3_f32 v50, v50, s72, v180
	v_med3_f32 v51, v51, s72, v180
	v_mov_b32_e32 v54, 0
	v_cvt_pk_fp8_f32 v54, v50, v51
	v_pk_mul_f32 v[50:51], v[52:53], s[48:49] op_sel_hi:[1,0]
	v_pk_mul_f32 v[46:47], v[46:47], s[48:49] op_sel_hi:[1,0]
	v_med3_f32 v50, v50, s72, v180
	v_med3_f32 v51, v51, s72, v180
	v_cvt_pk_fp8_f32 v54, v50, v51 op_sel:[0,0,1]
	v_med3_f32 v46, v46, s72, v180
	v_med3_f32 v47, v47, s72, v180
	v_mov_b32_e32 v50, 0
	v_cvt_pk_fp8_f32 v50, v46, v47
	v_pk_mul_f32 v[46:47], v[48:49], s[48:49] op_sel_hi:[1,0]
	v_pk_mul_f32 v[42:43], v[42:43], s[48:49] op_sel_hi:[1,0]
	v_med3_f32 v46, v46, s72, v180
	v_med3_f32 v47, v47, s72, v180
	v_cvt_pk_fp8_f32 v50, v46, v47 op_sel:[0,0,1]
	v_med3_f32 v42, v42, s72, v180
	v_med3_f32 v43, v43, s72, v180
	v_mov_b32_e32 v46, 0
	v_cvt_pk_fp8_f32 v46, v42, v43
	v_pk_mul_f32 v[42:43], v[44:45], s[48:49] op_sel_hi:[1,0]
	v_pk_mul_f32 v[38:39], v[38:39], s[48:49] op_sel_hi:[1,0]
	v_med3_f32 v42, v42, s72, v180
	v_med3_f32 v43, v43, s72, v180
	v_cvt_pk_fp8_f32 v46, v42, v43 op_sel:[0,0,1]
	v_med3_f32 v38, v38, s72, v180
	v_med3_f32 v39, v39, s72, v180
	v_mov_b32_e32 v42, 0
	v_cvt_pk_fp8_f32 v42, v38, v39
	v_pk_mul_f32 v[38:39], v[40:41], s[48:49] op_sel_hi:[1,0]
	v_pk_mul_f32 v[34:35], v[34:35], s[48:49] op_sel_hi:[1,0]
	v_med3_f32 v38, v38, s72, v180
	v_med3_f32 v39, v39, s72, v180
	v_cvt_pk_fp8_f32 v42, v38, v39 op_sel:[0,0,1]
	v_med3_f32 v34, v34, s72, v180
	v_med3_f32 v35, v35, s72, v180
	v_mov_b32_e32 v38, 0
	v_cvt_pk_fp8_f32 v38, v34, v35
	v_pk_mul_f32 v[34:35], v[36:37], s[48:49] op_sel_hi:[1,0]
	s_waitcnt lgkmcnt(0)
	s_nop 0
	v_med3_f32 v34, v34, s72, v180
	v_med3_f32 v35, v35, s72, v180
	v_cvt_pk_fp8_f32 v38, v34, v35 op_sel:[0,0,1]
	ds_write2_b32 v181, v66, v62 offset1:4
	ds_write2_b32 v181, v58, v54 offset0:8 offset1:12
	ds_write2_b32 v100, v50, v46 offset0:16 offset1:20
	ds_write2_b32 v100, v42, v38 offset0:24 offset1:28
	s_waitcnt lgkmcnt(0)
	s_and_saveexec_b64 s[22:23], s[14:15]
	s_cbranch_execz .LBB0_1208
	ds_read2_b32 v[34:35], v182 offset1:1
	ds_read2_b32 v[36:37], v182 offset0:2 offset1:3
	v_lshl_add_u64 v[38:39], v[122:123], 0, v[160:161]
	s_waitcnt lgkmcnt(0)
	global_store_dwordx4 v[38:39], v[34:37], off nt
; __device__ __forceinline__ int pack4_fp8(float a, float b, float c, float d) { int w = __builtin_amdgcn_cvt_pk_fp8_f32(a, b, 0, false); return __builtin_amdgcn_cvt_pk_fp8_f32(c, d, w, true); }
; __device__ void rt5b_stream(const Params& p, unsigned char* smem, const XMap& xm) {
;     ...
;                 if (wact) {
;                     unsigned char* stg = smem + 65536 + 32768 + wid * STG_WAVE;
;                     unsigned char* ybase = p.y + (j >> 1) * 256 + wc * 64;
; #pragma unroll
;                     for (int ps = 0; ps < 4; ++ps) {
;                         const int sl[2] = {ps == 0 ? sl00 : ps == 1 ? sl10 : ps == 2 ? sl20 : sl30, ps == 0 ? sl01 : ps == 1 ? sl11 : ps == 2 ? sl21 : sl31};
; #pragma unroll
;                         for (int mm = 0; mm < 2; ++mm)
; #pragma unroll
;                             for (int n = 0; n < 4; ++n) {
;                                 const f32x4 v = acc[ps * 2 + mm][n] * (16.0f / (A8S * D8S));
;                                 *(int*)(stg + (mm * 16 + l15) * 68 + n * 16 + gq * 4) = pack4_fp8(__builtin_amdgcn_fmed3f(v[0], -440.f, 440.f), __builtin_amdgcn_fmed3f(v[1], -440.f, 440.f), __builtin_amdgcn_fmed3f(v[2], -440.f, 440.f), __builtin_amdgcn_fmed3f(v[3], -440.f, 440.f));
;                             }
;                         asm volatile("s_waitcnt lgkmcnt(0)" ::: "memory");
; #pragma unroll
;                         for (int i2 = 0; i2 < 2; ++i2) {
;                             const int row = i2 * 16 + (lane >> 2), ch = lane & 3;
;                             const unsigned char* q = stg + row * 68 + ch * 16;
;                             uint4 w; w.x = *(const unsigned*)(q); w.y = *(const unsigned*)(q + 4); w.z = *(const unsigned*)(q + 8); w.w = *(const unsigned*)(q + 12);
;                             if (sl[i2] >= 0) *(uint4*)(ybase + (size_t)sl[i2] * D + ch * 16) = w;
;                         }
;                         asm volatile("s_waitcnt lgkmcnt(0)" ::: "memory");
;                     }
.LBB0_1208:
	s_or_b64 exec, exec, s[22:23]
	s_and_saveexec_b64 s[22:23], s[16:17]
	s_cbranch_execz .LBB0_1210
	ds_read2_b32 v[34:35], v98 offset1:1
	ds_read2_b32 v[36:37], v99 offset1:1
	v_lshl_add_u64 v[38:39], v[122:123], 0, v[162:163]
	s_waitcnt lgkmcnt(0)
	global_store_dwordx4 v[38:39], v[34:37], off nt
.LBB0_1210:
	s_or_b64 exec, exec, s[22:23]
	v_pk_mul_f32 v[30:31], v[30:31], s[48:49] op_sel_hi:[1,0]
	v_mov_b32_e32 v34, 0
	v_med3_f32 v30, v30, s72, v180
	v_med3_f32 v31, v31, s72, v180
	v_cvt_pk_fp8_f32 v34, v30, v31
	v_pk_mul_f32 v[30:31], v[32:33], s[48:49] op_sel_hi:[1,0]
	v_pk_mul_f32 v[26:27], v[26:27], s[48:49] op_sel_hi:[1,0]
	v_med3_f32 v30, v30, s72, v180
	v_med3_f32 v31, v31, s72, v180
	v_cvt_pk_fp8_f32 v34, v30, v31 op_sel:[0,0,1]
	v_med3_f32 v26, v26, s72, v180
	v_med3_f32 v27, v27, s72, v180
	v_mov_b32_e32 v30, 0
	v_cvt_pk_fp8_f32 v30, v26, v27
	v_pk_mul_f32 v[26:27], v[28:29], s[48:49] op_sel_hi:[1,0]
	v_pk_mul_f32 v[22:23], v[22:23], s[48:49] op_sel_hi:[1,0]
	v_med3_f32 v26, v26, s72, v180
	v_med3_f32 v27, v27, s72, v180
	v_cvt_pk_fp8_f32 v30, v26, v27 op_sel:[0,0,1]
	v_med3_f32 v22, v22, s72, v180
	v_med3_f32 v23, v23, s72, v180
	v_mov_b32_e32 v26, 0
	v_cvt_pk_fp8_f32 v26, v22, v23
	v_pk_mul_f32 v[22:23], v[24:25], s[48:49] op_sel_hi:[1,0]
	v_pk_mul_f32 v[18:19], v[18:19], s[48:49] op_sel_hi:[1,0]
	v_med3_f32 v22, v22, s72, v180
	v_med3_f32 v23, v23, s72, v180
	v_cvt_pk_fp8_f32 v26, v22, v23 op_sel:[0,0,1]
	v_med3_f32 v18, v18, s72, v180
	v_med3_f32 v19, v19, s72, v180
	v_mov_b32_e32 v22, 0
	v_cvt_pk_fp8_f32 v22, v18, v19
	v_pk_mul_f32 v[18:19], v[20:21], s[48:49] op_sel_hi:[1,0]
	v_pk_mul_f32 v[14:15], v[14:15], s[48:49] op_sel_hi:[1,0]
	v_med3_f32 v18, v18, s72, v180
	v_med3_f32 v19, v19, s72, v180
	v_cvt_pk_fp8_f32 v22, v18, v19 op_sel:[0,0,1]
	v_med3_f32 v14, v14, s72, v180
	v_med3_f32 v15, v15, s72, v180
	v_mov_b32_e32 v18, 0
	v_cvt_pk_fp8_f32 v18, v14, v15
	v_pk_mul_f32 v[14:15], v[16:17], s[48:49] op_sel_hi:[1,0]
	v_pk_mul_f32 v[10:11], v[10:11], s[48:49] op_sel_hi:[1,0]
	v_med3_f32 v14, v14, s72, v180
	v_med3_f32 v15, v15, s72, v180
	v_cvt_pk_fp8_f32 v18, v14, v15 op_sel:[0,0,1]
	v_med3_f32 v10, v10, s72, v180
	v_med3_f32 v11, v11, s72, v180
	v_mov_b32_e32 v14, 0
	v_cvt_pk_fp8_f32 v14, v10, v11
	v_pk_mul_f32 v[10:11], v[12:13], s[48:49] op_sel_hi:[1,0]
	v_pk_mul_f32 v[6:7], v[6:7], s[48:49] op_sel_hi:[1,0]
	v_med3_f32 v10, v10, s72, v180
	v_med3_f32 v11, v11, s72, v180
	v_cvt_pk_fp8_f32 v14, v10, v11 op_sel:[0,0,1]
	v_med3_f32 v6, v6, s72, v180
	v_med3_f32 v7, v7, s72, v180
	v_mov_b32_e32 v10, 0
	v_cvt_pk_fp8_f32 v10, v6, v7
	v_pk_mul_f32 v[6:7], v[8:9], s[48:49] op_sel_hi:[1,0]
	v_pk_mul_f32 v[2:3], v[2:3], s[48:49] op_sel_hi:[1,0]
	v_med3_f32 v6, v6, s72, v180
	v_med3_f32 v7, v7, s72, v180
	v_cvt_pk_fp8_f32 v10, v6, v7 op_sel:[0,0,1]
	v_med3_f32 v2, v2, s72, v180
	v_med3_f32 v3, v3, s72, v180
	v_mov_b32_e32 v6, 0
	v_cvt_pk_fp8_f32 v6, v2, v3
	v_pk_mul_f32 v[2:3], v[4:5], s[48:49] op_sel_hi:[1,0]
	s_waitcnt lgkmcnt(0)
	s_nop 0
	v_med3_f32 v2, v2, s72, v180
	v_med3_f32 v3, v3, s72, v180
	v_cvt_pk_fp8_f32 v6, v2, v3 op_sel:[0,0,1]
	ds_write2_b32 v181, v34, v30 offset1:4
	ds_write2_b32 v181, v26, v22 offset0:8 offset1:12
	ds_write2_b32 v100, v18, v14 offset0:16 offset1:20
	ds_write2_b32 v100, v10, v6 offset0:24 offset1:28
	s_waitcnt lgkmcnt(0)
	s_and_saveexec_b64 s[22:23], s[18:19]
	s_cbranch_execz .LBB0_1212
	ds_read2_b32 v[2:3], v182 offset1:1
	ds_read2_b32 v[4:5], v182 offset0:2 offset1:3
	v_lshl_add_u64 v[6:7], v[122:123], 0, v[164:165]
	s_waitcnt lgkmcnt(0)
	global_store_dwordx4 v[6:7], v[2:5], off nt
.LBB0_1212:
	s_or_b64 exec, exec, s[22:23]
	s_and_saveexec_b64 s[22:23], s[20:21]
	s_cbranch_execz .LBB0_1180
	ds_read2_b32 v[2:3], v98 offset1:1
	ds_read2_b32 v[4:5], v99 offset1:1
	v_lshl_add_u64 v[6:7], v[122:123], 0, v[166:167]
	s_waitcnt lgkmcnt(0)
	global_store_dwordx4 v[6:7], v[2:5], off nt
	s_branch .LBB0_1180
